# MoE1: gather-index loads for the unit after next issued without a wait; converted in K-loop iteration 2 after a counted wait
# speedup vs baseline: 1.0052x; 1.0052x over previous
;     __device__ __forceinline__ const char* a_base(const Unit& u) const { return (const char*)A + (size_t)u.pm * BM * lda * 2; }
;     __device__ __forceinline__ const char* b_base(const Unit& u) const { return (const char*)Bt + (size_t)u.pn * BM * K * 2; }
;     __device__ __forceinline__ const char* a_base(const Unit& u) const { const int b = u.pm >> 1, g = u.pm & 1; return (const char*)(z + (size_t)b * SEQ * ZP + (u.a0 ? ZC_VC : ZC_KC) + g * 64); }
;     __device__ __forceinline__ const char* b_base(const Unit& u) const { return (const char*)(u.a0 ? W1v : W1k); }
; template <class Epi, class Sched>
; __device__ __forceinline__ void gemm_phase(PG8_LAS unsigned char* lds, const int K, const Sched& S, const Epi& E, const int wave_s) {
;     ...
;         if (has_next) { nA = S.a_base(nxt); nB = S.b_base(nxt); S.a_voff(nxt, Rr, Cc, vN); }
;     __device__ __forceinline__ void a_voff(const Unit& u, const int (&R)[2], const int (&C)[2], unsigned (&v)[2][2]) const {
;         if (PHASE == 1) {
;             const int cnt = tab[80 + u.a0];
; #pragma unroll
;             for (int h = 0; h < 2; ++h)
; #pragma unroll
;                 for (int i = 0; i < 2; ++i) { const int rank = u.a1 * BM + h * HALF + R[i]; const int tok = rank < cnt ? ltok[(size_t)u.a0 * NTOK + rank] : 0; v[h][i] = (unsigned)(tok * DM + C[i]) * 2u; }
.LBB0_905:
	s_mov_b32 s101, 0
	v_cndmask_b32_e64 v2, 0, 1, s[22:23]
	v_cmp_ne_u32_e64 s[4:5], 1, v2
	s_andn2_b64 vcc, exec, s[22:23]
	s_mov_b64 s[22:23], s[28:29]
	v_mov_b32_e32 v161, v140
	v_mov_b32_e32 v158, v134
	v_mov_b32_e32 v159, v136
	v_mov_b32_e32 v160, v138
	s_cbranch_vccnz .LBB0_915
	s_lshl_b32 s19, s18, 2
	s_add_i32 s19, s19, 0
	s_add_i32 s19, s19, 0x24140
	v_mov_b32_e32 v2, s19
	ds_read_b32 v8, v2
	v_lshlrev_b32_e32 v9, 8, v157
	v_or_b32_e32 v11, 0x80, v9
	v_add_u32_e32 v20, v9, v147
	v_add_u32_e32 v21, v9, v149
	v_add_u32_e32 v22, v11, v147
	v_add_u32_e32 v23, v11, v149
	s_ashr_i32 s19, s18, 31
	s_lshl_b64 s[30:31], s[18:19], 18
	s_add_u32 s30, s41, s30
	s_addc_u32 s31, s42, s31
	v_mov_b32_e32 v12, v20
	v_mov_b32_e32 v13, 0
	v_mov_b32_e32 v14, v21
	v_mov_b32_e32 v15, 0
	v_mov_b32_e32 v16, v22
	v_mov_b32_e32 v17, 0
	v_mov_b32_e32 v18, v23
	v_mov_b32_e32 v19, 0
	v_lshl_add_u64 v[12:13], v[12:13], 2, s[30:31]
	v_lshl_add_u64 v[14:15], v[14:15], 2, s[30:31]
	v_lshl_add_u64 v[16:17], v[16:17], 2, s[30:31]
	v_lshl_add_u64 v[18:19], v[18:19], 2, s[30:31]
	v_mov_b32_e32 v158, 0
	v_mov_b32_e32 v159, 0
	v_mov_b32_e32 v160, 0
	v_mov_b32_e32 v161, 0
	s_mov_b32 s101, 1
	s_waitcnt lgkmcnt(0)
	v_cmp_lt_i32_e32 vcc, v20, v8
	s_nop 0
	s_and_saveexec_b64 s[22:23], vcc
	global_load_dword v160, v[12:13], off
	s_or_b64 exec, exec, s[22:23]
	v_cmp_lt_i32_e32 vcc, v21, v8
	s_nop 0
	s_and_saveexec_b64 s[22:23], vcc
	global_load_dword v159, v[14:15], off
	s_or_b64 exec, exec, s[22:23]
	v_cmp_lt_i32_e32 vcc, v22, v8
	s_nop 0
	s_and_saveexec_b64 s[22:23], vcc
	global_load_dword v158, v[16:17], off
	s_or_b64 exec, exec, s[22:23]
	v_cmp_lt_i32_e32 vcc, v23, v8
	s_nop 0
	s_and_saveexec_b64 s[22:23], vcc
	global_load_dword v161, v[18:19], off
	s_or_b64 exec, exec, s[22:23]
	s_lshl_b32 s19, s18, 21
	s_ashr_i32 s21, s20, 31
	s_and_b32 s19, s19, 0x3e00000
	s_lshl_b64 s[22:23], s[20:21], 19
	s_add_u32 s21, s43, s22
	s_addc_u32 s23, s44, s23
	s_add_u32 s22, s21, s19
	s_addc_u32 s23, s23, 0

; #define PG8_STAGE(bufoff, gbase, voff) do { _Pragma("unroll") for (int _i = 0; _i < 2; ++_i) \
;         __builtin_amdgcn_global_load_lds((const unsigned*)((const char*)(gbase) + (voff)[_i]), (PG8_LAS unsigned*)(lds + (bufoff) + ldsw + _i * 8192), 16, 0, 0); } while (0)
; #define PG8_LDA(dst, b, h) do { _Pragma("unroll") for (int m = 0; m < 4; ++m) _Pragma("unroll") for (int k = 0; k < 2; ++k) dst[m][k] = *(const PG8_LAS bf16x8*)(lds + PG8_SA(b, h) + aoff + m * 2048 + k * 1024); } while (0)
; #define PG8_LDB(dst, b, h) do { _Pragma("unroll") for (int n = 0; n < 2; ++n) _Pragma("unroll") for (int k = 0; k < 2; ++k) dst[n][k] = *(const PG8_LAS bf16x8*)(lds + PG8_SB(b, h) + boff + n * 2048 + k * 1024); } while (0)
; #define PG8_MMA(ai, bj, At, Bt) do { __builtin_amdgcn_s_setprio(1); _Pragma("unroll") for (int m = 0; m < 4; ++m) _Pragma("unroll") for (int n = 0; n < 2; ++n) _Pragma("unroll") for (int k = 0; k < 2; ++k) \
;         acc[ai][bj][m][n] = __builtin_amdgcn_mfma_f32_16x16x32_bf16(Bt[n][k], At[m][k], acc[ai][bj][m][n], 0, 0, 0); __builtin_amdgcn_s_setprio(0); } while (0)
; #define PG8_WAIT_V(n) asm volatile("s_waitcnt vmcnt(" #n ")" ::: "memory")
; #define PG8_WAIT_L(n) asm volatile("s_waitcnt lgkmcnt(" #n ")" ::: "memory")
; #define PG8_BAR __builtin_amdgcn_s_barrier()
; #define PG8_SCHED __builtin_amdgcn_sched_barrier(0)
; template <class Epi, class Sched>
; __device__ __forceinline__ void gemm_phase(PG8_LAS unsigned char* lds, const int K, const Sched& S, const Epi& E, const int wave_s) {
;     ...
;                 for (int i = 0; i < 2; ++i) v2[h][i] = last ? vN[h][i] : vA[h][i];
;             PG8_LDB(B0, 0, 0); PG8_LDB(B1, 0, 1); PG8_SCHED; PG8_LDA(At, 0, 0); PG8_STAGE(PG8_SA(1, 1), a1, vA[1]);
;             PG8_WAIT_V(8); PG8_WAIT_L(0); PG8_BAR; PG8_MMA(0, 0, At, B0); PG8_MMA(0, 1, At, B1); PG8_BAR; PG8_SCHED;
;             PG8_LDA(At, 0, 1); PG8_STAGE(PG8_SB(0, 0), b2, voffB); PG8_STAGE(PG8_SB(0, 1), b2 + hstepB, voffB); PG8_STAGE(PG8_SA(0, 0), a2, v2[0]);
;             PG8_WAIT_V(8); PG8_WAIT_L(0); PG8_BAR; PG8_MMA(1, 0, At, B0); PG8_MMA(1, 1, At, B1); PG8_BAR; PG8_SCHED;
.LBB0_916:
	s_add_u32 s27, s8, s28
	s_addc_u32 s30, s9, s29
	s_add_u32 s27, s27, 0x100
	s_addc_u32 s34, s30, 0
	s_add_u32 s57, s19, s28
	s_addc_u32 s58, s21, s29
	s_cmpk_eq_i32 s28, 0x700
	s_cselect_b64 vcc, -1, 0
	s_and_b64 s[30:31], vcc, exec
	s_cselect_b32 s35, s9, s34
	s_cselect_b32 s34, s8, s27
	s_cselect_b32 s31, s23, s58
	s_cselect_b32 s30, s22, s57
	s_add_i32 s27, 0, 0x10000
	v_add_u32_e32 v148, s27, v139
	s_add_i32 s57, 0, 0x14000
	ds_read_b128 v[162:165], v148
	ds_read_b128 v[166:169], v148 offset:1024
	ds_read_b128 v[170:173], v148 offset:2048
	ds_read_b128 v[174:177], v148 offset:3072
	v_add_u32_e32 v148, s57, v139
	ds_read_b128 v[178:181], v148
	ds_read_b128 v[182:185], v148 offset:1024
	ds_read_b128 v[192:195], v148 offset:2048
	ds_read_b128 v[196:199], v148 offset:3072
	v_cndmask_b32_e32 v150, v138, v160, vcc
	v_cndmask_b32_e32 v204, v136, v159, vcc
	v_cndmask_b32_e32 v135, v134, v158, vcc
	v_cndmask_b32_e32 v141, v140, v161, vcc
	v_lshl_add_u64 v[218:219], v[144:145], 0, s[28:29]
	s_add_i32 m0, s46, 0xc000
	ds_read_b128 v[200:203], v156
	ds_read_b128 v[222:225], v156 offset:1024
	ds_read_b128 v[226:229], v156 offset:2048
	ds_read_b128 v[230:233], v156 offset:3072
	ds_read_b128 v[234:237], v156 offset:4096
	ds_read_b128 v[238:241], v156 offset:5120
	ds_read_b128 v[242:245], v156 offset:6144
	ds_read_b128 v[246:249], v156 offset:7168
	global_load_lds_dwordx4 v[218:219], off
	v_lshl_add_u64 v[218:219], v[142:143], 0, s[28:29]
	s_add_i32 m0, s46, 0xe000
	s_nop 0
	global_load_lds_dwordx4 v[218:219], off
	s_waitcnt vmcnt(8)
	s_cmpk_eq_i32 s28, 0x100
	s_cbranch_scc0 .Lm1_nopost
	s_cmp_eq_u32 s101, 0
	s_cbranch_scc1 .Lm1_nopost
	v_lshlrev_b32_e32 v160, 10, v160
	v_lshlrev_b32_e32 v159, 10, v159
	v_lshlrev_b32_e32 v158, 10, v158
	v_lshlrev_b32_e32 v161, 10, v161
	v_add_lshl_u32 v160, v160, v153, 1
	v_add_lshl_u32 v159, v159, v154, 1
	v_add_lshl_u32 v158, v158, v153, 1
	v_add_lshl_u32 v161, v161, v154, 1
.Lm1_nopost:
	s_waitcnt lgkmcnt(0)
	s_barrier
	s_setprio 1
	s_waitcnt lgkmcnt(0)
	v_mfma_f32_16x16x32_bf16 v[126:129], v[162:165], v[200:203], v[126:129]
	v_mfma_f32_16x16x32_bf16 v[118:121], v[170:173], v[200:203], v[118:121]
	v_mfma_f32_16x16x32_bf16 v[110:113], v[162:165], v[226:229], v[110:113]
	v_mfma_f32_16x16x32_bf16 v[102:105], v[170:173], v[226:229], v[102:105]
	v_mfma_f32_16x16x32_bf16 v[94:97], v[162:165], v[234:237], v[94:97]
	v_mfma_f32_16x16x32_bf16 v[86:89], v[170:173], v[234:237], v[86:89]
	v_mfma_f32_16x16x32_bf16 v[78:81], v[162:165], v[242:245], v[78:81]
	v_mfma_f32_16x16x32_bf16 v[70:73], v[170:173], v[242:245], v[70:73]
	v_mfma_f32_16x16x32_bf16 v[126:129], v[166:169], v[222:225], v[126:129]
	v_mfma_f32_16x16x32_bf16 v[118:121], v[174:177], v[222:225], v[118:121]
	v_mfma_f32_16x16x32_bf16 v[110:113], v[166:169], v[230:233], v[110:113]
	v_mfma_f32_16x16x32_bf16 v[102:105], v[174:177], v[230:233], v[102:105]
	v_mfma_f32_16x16x32_bf16 v[94:97], v[166:169], v[238:241], v[94:97]
	v_mfma_f32_16x16x32_bf16 v[86:89], v[174:177], v[238:241], v[86:89]
	v_mfma_f32_16x16x32_bf16 v[78:81], v[166:169], v[246:249], v[78:81]
	v_mfma_f32_16x16x32_bf16 v[70:73], v[174:177], v[246:249], v[70:73]
	s_setprio 0
	s_setprio 1
	v_mfma_f32_16x16x32_bf16 v[122:125], v[178:181], v[200:203], v[122:125]
	v_mfma_f32_16x16x32_bf16 v[114:117], v[192:195], v[200:203], v[114:117]
	v_mfma_f32_16x16x32_bf16 v[106:109], v[178:181], v[226:229], v[106:109]
	v_mfma_f32_16x16x32_bf16 v[98:101], v[192:195], v[226:229], v[98:101]
	v_mfma_f32_16x16x32_bf16 v[90:93], v[178:181], v[234:237], v[90:93]
	v_mfma_f32_16x16x32_bf16 v[82:85], v[192:195], v[234:237], v[82:85]
	v_mfma_f32_16x16x32_bf16 v[74:77], v[178:181], v[242:245], v[74:77]
	v_mfma_f32_16x16x32_bf16 v[66:69], v[192:195], v[242:245], v[66:69]
	v_mfma_f32_16x16x32_bf16 v[122:125], v[182:185], v[222:225], v[122:125]
	v_mfma_f32_16x16x32_bf16 v[114:117], v[196:199], v[222:225], v[114:117]
	v_mfma_f32_16x16x32_bf16 v[106:109], v[182:185], v[230:233], v[106:109]
	v_mfma_f32_16x16x32_bf16 v[98:101], v[196:199], v[230:233], v[98:101]
	v_mfma_f32_16x16x32_bf16 v[90:93], v[182:185], v[238:241], v[90:93]
	v_mfma_f32_16x16x32_bf16 v[82:85], v[196:199], v[238:241], v[82:85]
	v_mfma_f32_16x16x32_bf16 v[74:77], v[182:185], v[246:249], v[74:77]
	v_mfma_f32_16x16x32_bf16 v[66:69], v[196:199], v[246:249], v[66:69]
	s_setprio 0
	s_barrier
	s_add_i32 s27, s27, s45
	v_lshl_add_u64 v[218:219], s[30:31], 0, v[130:131]
	s_mov_b32 m0, s27
	ds_read_b128 v[200:203], v156 offset:16384
	ds_read_b128 v[222:225], v156 offset:17408
	ds_read_b128 v[226:229], v156 offset:18432
	ds_read_b128 v[230:233], v156 offset:19456
	ds_read_b128 v[234:237], v156 offset:20480
	ds_read_b128 v[238:241], v156 offset:21504
	ds_read_b128 v[242:245], v156 offset:22528
	ds_read_b128 v[246:249], v156 offset:23552
	global_load_lds_dwordx4 v[218:219], off
	s_add_i32 m0, s27, 0x2000
	s_add_u32 s58, s30, 0x40000
	v_lshl_add_u64 v[220:221], s[30:31], 0, v[132:133]
	s_addc_u32 s59, s31, 0
	s_add_i32 s27, s57, s45
	global_load_lds_dwordx4 v[220:221], off
	v_lshl_add_u64 v[250:251], s[58:59], 0, v[130:131]
	s_mov_b32 m0, s27
	v_mov_b32_e32 v151, v0
	global_load_lds_dwordx4 v[250:251], off
	v_lshl_add_u64 v[250:251], s[58:59], 0, v[132:133]
	s_add_i32 m0, s27, 0x2000
	v_mov_b32_e32 v205, v0
	global_load_lds_dwordx4 v[250:251], off
	s_mov_b32 m0, s46
	s_nop 0
	global_load_lds_dwordx4 v150, s[34:35]
	s_mov_b32 m0, s47
	v_lshl_add_u64 v[150:151], s[34:35], 0, v[150:151]
	global_load_lds_dwordx4 v204, s[34:35]
	s_waitcnt vmcnt(8)
	s_waitcnt lgkmcnt(0)
	v_lshl_add_u64 v[204:205], s[34:35], 0, v[204:205]
	s_barrier
; #define PG8_STAGE(bufoff, gbase, voff) do { _Pragma("unroll") for (int _i = 0; _i < 2; ++_i) \
;         __builtin_amdgcn_global_load_lds((const unsigned*)((const char*)(gbase) + (voff)[_i]), (PG8_LAS unsigned*)(lds + (bufoff) + ldsw + _i * 8192), 16, 0, 0); } while (0)
; #define PG8_LDA(dst, b, h) do { _Pragma("unroll") for (int m = 0; m < 4; ++m) _Pragma("unroll") for (int k = 0; k < 2; ++k) dst[m][k] = *(const PG8_LAS bf16x8*)(lds + PG8_SA(b, h) + aoff + m * 2048 + k * 1024); } while (0)
; #define PG8_LDB(dst, b, h) do { _Pragma("unroll") for (int n = 0; n < 2; ++n) _Pragma("unroll") for (int k = 0; k < 2; ++k) dst[n][k] = *(const PG8_LAS bf16x8*)(lds + PG8_SB(b, h) + boff + n * 2048 + k * 1024); } while (0)
; #define PG8_MMA(ai, bj, At, Bt) do { __builtin_amdgcn_s_setprio(1); _Pragma("unroll") for (int m = 0; m < 4; ++m) _Pragma("unroll") for (int n = 0; n < 2; ++n) _Pragma("unroll") for (int k = 0; k < 2; ++k) \
;         acc[ai][bj][m][n] = __builtin_amdgcn_mfma_f32_16x16x32_bf16(Bt[n][k], At[m][k], acc[ai][bj][m][n], 0, 0, 0); __builtin_amdgcn_s_setprio(0); } while (0)
; #define PG8_WAIT_V(n) asm volatile("s_waitcnt vmcnt(" #n ")" ::: "memory")
; #define PG8_WAIT_L(n) asm volatile("s_waitcnt lgkmcnt(" #n ")" ::: "memory")
; #define PG8_BAR __builtin_amdgcn_s_barrier()
; #define PG8_SCHED __builtin_amdgcn_sched_barrier(0)
; template <class Epi, class Sched>
; __device__ __forceinline__ void gemm_phase(PG8_LAS unsigned char* lds, const int K, const Sched& S, const Epi& E, const int wave_s) {
;     ...
;             PG8_WAIT_V(8); PG8_WAIT_L(0); PG8_BAR; PG8_MMA(0, 0, At, B0); PG8_MMA(0, 1, At, B1); PG8_BAR; PG8_SCHED;
;             PG8_LDA(At, 0, 1); PG8_STAGE(PG8_SB(0, 0), b2, voffB); PG8_STAGE(PG8_SB(0, 1), b2 + hstepB, voffB); PG8_STAGE(PG8_SA(0, 0), a2, v2[0]);
;             PG8_WAIT_V(8); PG8_WAIT_L(0); PG8_BAR; PG8_MMA(1, 0, At, B0); PG8_MMA(1, 1, At, B1); PG8_BAR; PG8_SCHED;
;             PG8_LDB(B0, 1, 0); PG8_LDB(B1, 1, 1); PG8_SCHED; PG8_LDA(At, 1, 0); PG8_STAGE(PG8_SA(0, 1), a2, v2[1]);
;             PG8_WAIT_V(8); PG8_WAIT_L(0); PG8_BAR; PG8_MMA(0, 0, At, B0); PG8_MMA(0, 1, At, B1); PG8_BAR; PG8_SCHED;
	s_setprio 1
	s_waitcnt lgkmcnt(0)
	v_mfma_f32_16x16x32_bf16 v[62:65], v[162:165], v[200:203], v[62:65]
	v_mfma_f32_16x16x32_bf16 v[54:57], v[170:173], v[200:203], v[54:57]
	v_mfma_f32_16x16x32_bf16 v[46:49], v[162:165], v[226:229], v[46:49]
	v_mfma_f32_16x16x32_bf16 v[38:41], v[170:173], v[226:229], v[38:41]
	v_mfma_f32_16x16x32_bf16 v[26:29], v[162:165], v[234:237], v[26:29]
	v_mfma_f32_16x16x32_bf16 v[18:21], v[170:173], v[234:237], v[18:21]
	v_mfma_f32_16x16x32_bf16 v[10:13], v[162:165], v[242:245], v[10:13]
	v_mfma_f32_16x16x32_bf16 v[2:5], v[170:173], v[242:245], v[2:5]
	v_mfma_f32_16x16x32_bf16 v[62:65], v[166:169], v[222:225], v[62:65]
	v_mfma_f32_16x16x32_bf16 v[54:57], v[174:177], v[222:225], v[54:57]
	v_mfma_f32_16x16x32_bf16 v[46:49], v[166:169], v[230:233], v[46:49]
	v_mfma_f32_16x16x32_bf16 v[38:41], v[174:177], v[230:233], v[38:41]
	v_mfma_f32_16x16x32_bf16 v[26:29], v[166:169], v[238:241], v[26:29]
	v_mfma_f32_16x16x32_bf16 v[18:21], v[174:177], v[238:241], v[18:21]
	v_mfma_f32_16x16x32_bf16 v[10:13], v[166:169], v[246:249], v[10:13]
	v_mfma_f32_16x16x32_bf16 v[2:5], v[174:177], v[246:249], v[2:5]
	s_setprio 0
	s_setprio 1
	v_mfma_f32_16x16x32_bf16 v[58:61], v[178:181], v[200:203], v[58:61]
	v_mfma_f32_16x16x32_bf16 v[50:53], v[192:195], v[200:203], v[50:53]
	v_mfma_f32_16x16x32_bf16 v[42:45], v[178:181], v[226:229], v[42:45]
	v_mfma_f32_16x16x32_bf16 v[34:37], v[192:195], v[226:229], v[34:37]
	v_mfma_f32_16x16x32_bf16 v[30:33], v[178:181], v[234:237], v[30:33]
	v_mfma_f32_16x16x32_bf16 v[22:25], v[192:195], v[234:237], v[22:25]
	v_mfma_f32_16x16x32_bf16 v[14:17], v[178:181], v[242:245], v[14:17]
	v_mfma_f32_16x16x32_bf16 v[6:9], v[192:195], v[242:245], v[6:9]
	v_mfma_f32_16x16x32_bf16 v[58:61], v[182:185], v[222:225], v[58:61]
	v_mfma_f32_16x16x32_bf16 v[50:53], v[196:199], v[222:225], v[50:53]
	v_mfma_f32_16x16x32_bf16 v[42:45], v[182:185], v[230:233], v[42:45]
	v_mfma_f32_16x16x32_bf16 v[34:37], v[196:199], v[230:233], v[34:37]
	v_mfma_f32_16x16x32_bf16 v[30:33], v[182:185], v[238:241], v[30:33]
	v_mfma_f32_16x16x32_bf16 v[22:25], v[196:199], v[238:241], v[22:25]
	v_mfma_f32_16x16x32_bf16 v[14:17], v[182:185], v[246:249], v[14:17]
	v_mfma_f32_16x16x32_bf16 v[6:9], v[196:199], v[246:249], v[6:9]
	s_setprio 0
	s_barrier
	s_add_i32 s27, 0, 0x18000
	v_add_u32_e32 v148, s27, v139
	s_add_i32 s57, 0, 0x1c000
	ds_read_b128 v[162:165], v148
	ds_read_b128 v[166:169], v148 offset:1024
	ds_read_b128 v[170:173], v148 offset:2048
	ds_read_b128 v[174:177], v148 offset:3072
	v_add_u32_e32 v148, s57, v139
	ds_read_b128 v[178:181], v148
	ds_read_b128 v[182:185], v148 offset:1024
	ds_read_b128 v[192:195], v148 offset:2048
	ds_read_b128 v[196:199], v148 offset:3072
	s_mov_b32 m0, s48
	ds_read_b128 v[200:203], v156 offset:32768
	ds_read_b128 v[222:225], v156 offset:33792
	ds_read_b128 v[226:229], v156 offset:34816
	ds_read_b128 v[230:233], v156 offset:35840
	ds_read_b128 v[234:237], v156 offset:36864
	ds_read_b128 v[238:241], v156 offset:37888
	ds_read_b128 v[242:245], v156 offset:38912
	ds_read_b128 v[246:249], v156 offset:39936
	global_load_lds_dwordx4 v135, s[34:35]
	s_mov_b32 m0, s49
	s_nop 0
	global_load_lds_dwordx4 v141, s[34:35]
	s_waitcnt vmcnt(8)
	s_waitcnt lgkmcnt(0)
	s_barrier
	s_setprio 1
	s_waitcnt lgkmcnt(0)
	v_mfma_f32_16x16x32_bf16 v[126:129], v[162:165], v[200:203], v[126:129]
	v_mfma_f32_16x16x32_bf16 v[118:121], v[170:173], v[200:203], v[118:121]
	v_mfma_f32_16x16x32_bf16 v[110:113], v[162:165], v[226:229], v[110:113]
	v_mfma_f32_16x16x32_bf16 v[102:105], v[170:173], v[226:229], v[102:105]
	v_mfma_f32_16x16x32_bf16 v[94:97], v[162:165], v[234:237], v[94:97]
	v_mfma_f32_16x16x32_bf16 v[86:89], v[170:173], v[234:237], v[86:89]
	v_mfma_f32_16x16x32_bf16 v[78:81], v[162:165], v[242:245], v[78:81]
	v_mfma_f32_16x16x32_bf16 v[70:73], v[170:173], v[242:245], v[70:73]
	v_mfma_f32_16x16x32_bf16 v[126:129], v[166:169], v[222:225], v[126:129]
	v_mfma_f32_16x16x32_bf16 v[118:121], v[174:177], v[222:225], v[118:121]
	v_mfma_f32_16x16x32_bf16 v[110:113], v[166:169], v[230:233], v[110:113]
	v_mfma_f32_16x16x32_bf16 v[102:105], v[174:177], v[230:233], v[102:105]
	v_mfma_f32_16x16x32_bf16 v[94:97], v[166:169], v[238:241], v[94:97]
	v_mfma_f32_16x16x32_bf16 v[86:89], v[174:177], v[238:241], v[86:89]
	v_mfma_f32_16x16x32_bf16 v[78:81], v[166:169], v[246:249], v[78:81]
	v_mfma_f32_16x16x32_bf16 v[70:73], v[174:177], v[246:249], v[70:73]
	s_setprio 0
	s_setprio 1
	v_mfma_f32_16x16x32_bf16 v[122:125], v[178:181], v[200:203], v[122:125]
	v_mfma_f32_16x16x32_bf16 v[114:117], v[192:195], v[200:203], v[114:117]
	v_mfma_f32_16x16x32_bf16 v[106:109], v[178:181], v[226:229], v[106:109]
	v_mfma_f32_16x16x32_bf16 v[98:101], v[192:195], v[226:229], v[98:101]
	v_mfma_f32_16x16x32_bf16 v[90:93], v[178:181], v[234:237], v[90:93]
	v_mfma_f32_16x16x32_bf16 v[82:85], v[192:195], v[234:237], v[82:85]
	v_mfma_f32_16x16x32_bf16 v[74:77], v[178:181], v[242:245], v[74:77]
	v_mfma_f32_16x16x32_bf16 v[66:69], v[192:195], v[242:245], v[66:69]
	v_mfma_f32_16x16x32_bf16 v[122:125], v[182:185], v[222:225], v[122:125]
	v_mfma_f32_16x16x32_bf16 v[114:117], v[196:199], v[222:225], v[114:117]
	v_mfma_f32_16x16x32_bf16 v[106:109], v[182:185], v[230:233], v[106:109]
	v_mfma_f32_16x16x32_bf16 v[98:101], v[196:199], v[230:233], v[98:101]
	v_mfma_f32_16x16x32_bf16 v[90:93], v[182:185], v[238:241], v[90:93]
	v_mfma_f32_16x16x32_bf16 v[82:85], v[196:199], v[238:241], v[82:85]
	v_mfma_f32_16x16x32_bf16 v[74:77], v[182:185], v[246:249], v[74:77]
	v_mfma_f32_16x16x32_bf16 v[66:69], v[196:199], v[246:249], v[66:69]
	s_setprio 0
	s_barrier
; #define PG8_STAGE(bufoff, gbase, voff) do { _Pragma("unroll") for (int _i = 0; _i < 2; ++_i) \
;         __builtin_amdgcn_global_load_lds((const unsigned*)((const char*)(gbase) + (voff)[_i]), (PG8_LAS unsigned*)(lds + (bufoff) + ldsw + _i * 8192), 16, 0, 0); } while (0)
; #define PG8_LDA(dst, b, h) do { _Pragma("unroll") for (int m = 0; m < 4; ++m) _Pragma("unroll") for (int k = 0; k < 2; ++k) dst[m][k] = *(const PG8_LAS bf16x8*)(lds + PG8_SA(b, h) + aoff + m * 2048 + k * 1024); } while (0)
; #define PG8_MMA(ai, bj, At, Bt) do { __builtin_amdgcn_s_setprio(1); _Pragma("unroll") for (int m = 0; m < 4; ++m) _Pragma("unroll") for (int n = 0; n < 2; ++n) _Pragma("unroll") for (int k = 0; k < 2; ++k) \
;         acc[ai][bj][m][n] = __builtin_amdgcn_mfma_f32_16x16x32_bf16(Bt[n][k], At[m][k], acc[ai][bj][m][n], 0, 0, 0); __builtin_amdgcn_s_setprio(0); } while (0)
; #define PG8_WAIT_V(n) asm volatile("s_waitcnt vmcnt(" #n ")" ::: "memory")
; #define PG8_WAIT_L(n) asm volatile("s_waitcnt lgkmcnt(" #n ")" ::: "memory")
; #define PG8_BAR __builtin_amdgcn_s_barrier()
; #define PG8_SCHED __builtin_amdgcn_sched_barrier(0)
; template <class Epi, class Sched>
; __device__ __forceinline__ void gemm_phase(PG8_LAS unsigned char* lds, const int K, const Sched& S, const Epi& E, const int wave_s) {
;     ...
;             PG8_WAIT_V(8); PG8_WAIT_L(0); PG8_BAR; PG8_MMA(0, 0, At, B0); PG8_MMA(0, 1, At, B1); PG8_BAR; PG8_SCHED;
;             PG8_LDA(At, 1, 1); PG8_STAGE(PG8_SB(1, 0), b3, voffB); PG8_STAGE(PG8_SB(1, 1), b3 + hstepB, voffB); PG8_STAGE(PG8_SA(1, 0), a3, v2[0]);
;             PG8_WAIT_V(8); PG8_WAIT_L(0); PG8_BAR; PG8_MMA(1, 0, At, B0); PG8_MMA(1, 1, At, B1); PG8_BAR; PG8_SCHED;
;         }
;         if (wr == 0) PG8_BAR;
	s_add_i32 s27, s27, s45
	v_lshl_add_u64 v[218:219], v[218:219], 0, s[60:61]
	s_mov_b32 m0, s27
	ds_read_b128 v[200:203], v156 offset:49152
	ds_read_b128 v[222:225], v156 offset:50176
	ds_read_b128 v[226:229], v156 offset:51200
	ds_read_b128 v[230:233], v156 offset:52224
	ds_read_b128 v[234:237], v156 offset:53248
	ds_read_b128 v[238:241], v156 offset:54272
	ds_read_b128 v[242:245], v156 offset:55296
	ds_read_b128 v[246:249], v156 offset:56320
	global_load_lds_dwordx4 v[218:219], off
	s_add_i32 m0, s27, 0x2000
	s_add_u32 s30, s30, 0x40080
	v_lshl_add_u64 v[218:219], v[220:221], 0, s[60:61]
	s_addc_u32 s31, s31, 0
	s_add_i32 s27, s57, s45
	global_load_lds_dwordx4 v[218:219], off
	v_lshl_add_u64 v[218:219], s[30:31], 0, v[130:131]
	s_mov_b32 m0, s27
	v_lshl_add_u64 v[150:151], v[150:151], 0, s[60:61]
	global_load_lds_dwordx4 v[218:219], off
	v_lshl_add_u64 v[218:219], s[30:31], 0, v[132:133]
	s_add_i32 m0, s27, 0x2000
	s_nop 0
	global_load_lds_dwordx4 v[218:219], off
	s_mov_b32 m0, s52
	s_nop 0
	global_load_lds_dwordx4 v[150:151], off
	v_lshl_add_u64 v[150:151], v[204:205], 0, s[60:61]
	s_mov_b32 m0, s53
	s_nop 0
	global_load_lds_dwordx4 v[150:151], off
	s_waitcnt vmcnt(8)
	s_waitcnt lgkmcnt(0)
	s_barrier
	s_setprio 1
	s_waitcnt lgkmcnt(0)
	v_mfma_f32_16x16x32_bf16 v[62:65], v[162:165], v[200:203], v[62:65]
	v_mfma_f32_16x16x32_bf16 v[54:57], v[170:173], v[200:203], v[54:57]
	v_mfma_f32_16x16x32_bf16 v[46:49], v[162:165], v[226:229], v[46:49]
	v_mfma_f32_16x16x32_bf16 v[38:41], v[170:173], v[226:229], v[38:41]
	v_mfma_f32_16x16x32_bf16 v[26:29], v[162:165], v[234:237], v[26:29]
	v_mfma_f32_16x16x32_bf16 v[18:21], v[170:173], v[234:237], v[18:21]
	v_mfma_f32_16x16x32_bf16 v[10:13], v[162:165], v[242:245], v[10:13]
	v_mfma_f32_16x16x32_bf16 v[2:5], v[170:173], v[242:245], v[2:5]
	v_mfma_f32_16x16x32_bf16 v[62:65], v[166:169], v[222:225], v[62:65]
	v_mfma_f32_16x16x32_bf16 v[54:57], v[174:177], v[222:225], v[54:57]
	v_mfma_f32_16x16x32_bf16 v[46:49], v[166:169], v[230:233], v[46:49]
	v_mfma_f32_16x16x32_bf16 v[38:41], v[174:177], v[230:233], v[38:41]
	v_mfma_f32_16x16x32_bf16 v[26:29], v[166:169], v[238:241], v[26:29]
	v_mfma_f32_16x16x32_bf16 v[18:21], v[174:177], v[238:241], v[18:21]
	v_mfma_f32_16x16x32_bf16 v[10:13], v[166:169], v[246:249], v[10:13]
	v_mfma_f32_16x16x32_bf16 v[2:5], v[174:177], v[246:249], v[2:5]
	s_setprio 0
	s_setprio 1
	v_mfma_f32_16x16x32_bf16 v[58:61], v[178:181], v[200:203], v[58:61]
	v_mfma_f32_16x16x32_bf16 v[50:53], v[192:195], v[200:203], v[50:53]
	v_mfma_f32_16x16x32_bf16 v[42:45], v[178:181], v[226:229], v[42:45]
	v_mfma_f32_16x16x32_bf16 v[34:37], v[192:195], v[226:229], v[34:37]
	v_mfma_f32_16x16x32_bf16 v[30:33], v[178:181], v[234:237], v[30:33]
	v_mfma_f32_16x16x32_bf16 v[22:25], v[192:195], v[234:237], v[22:25]
	v_mfma_f32_16x16x32_bf16 v[14:17], v[178:181], v[242:245], v[14:17]
	v_mfma_f32_16x16x32_bf16 v[6:9], v[192:195], v[242:245], v[6:9]
	v_mfma_f32_16x16x32_bf16 v[58:61], v[182:185], v[222:225], v[58:61]
	v_mfma_f32_16x16x32_bf16 v[50:53], v[196:199], v[222:225], v[50:53]
	v_mfma_f32_16x16x32_bf16 v[42:45], v[182:185], v[230:233], v[42:45]
	v_mfma_f32_16x16x32_bf16 v[34:37], v[196:199], v[230:233], v[34:37]
	v_mfma_f32_16x16x32_bf16 v[30:33], v[182:185], v[238:241], v[30:33]
	v_mfma_f32_16x16x32_bf16 v[22:25], v[196:199], v[238:241], v[22:25]
	v_mfma_f32_16x16x32_bf16 v[14:17], v[182:185], v[246:249], v[14:17]
	v_mfma_f32_16x16x32_bf16 v[6:9], v[196:199], v[246:249], v[6:9]
	s_setprio 0
	s_barrier
	s_add_i32 s25, s25, 2
	s_add_u32 s28, s28, 0x100
	s_addc_u32 s29, s29, 0
	s_cmp_gt_u32 s25, 13
	s_cbranch_scc0 .LBB0_916
	s_and_b64 vcc, exec, s[14:15]
	s_cbranch_vccz .LBB0_919
	s_barrier

; #define LAS __attribute__((address_space(3)))
; __global__ void __launch_bounds__(NWAVES * 64, 2) fwd_kernel(Args args) {
;     extern __shared__ __attribute__((aligned(16))) unsigned char lds_raw[];
;     LAS unsigned char* lds = (LAS unsigned char*)lds_raw;
;     volatile LAS unsigned* MISC = (volatile LAS unsigned*)(lds + MISC_OFF);
;     const int G0 = gridDim.x, bid0 = blockIdx.x;
;     const int wave_s = __builtin_amdgcn_readfirstlane(threadIdx.x >> 6);
	.amdhsa_kernel _Z10fwd_kernel4Args
		.amdhsa_group_segment_fixed_size 0
		.amdhsa_private_segment_fixed_size 0
		.amdhsa_kernarg_size 576
		.amdhsa_user_sgpr_count 2
		.amdhsa_user_sgpr_dispatch_ptr 0
		.amdhsa_user_sgpr_queue_ptr 0
		.amdhsa_user_sgpr_kernarg_segment_ptr 1
		.amdhsa_user_sgpr_dispatch_id 0
		.amdhsa_user_sgpr_kernarg_preload_length 0
		.amdhsa_user_sgpr_kernarg_preload_offset 0
		.amdhsa_user_sgpr_private_segment_size 0
		.amdhsa_uses_dynamic_stack 0
		.amdhsa_enable_private_segment 0
		.amdhsa_system_sgpr_workgroup_id_x 1
		.amdhsa_system_sgpr_workgroup_id_y 0
		.amdhsa_system_sgpr_workgroup_id_z 0
		.amdhsa_system_sgpr_workgroup_info 0
		.amdhsa_system_vgpr_workitem_id 0
		.amdhsa_next_free_vgpr 256
		.amdhsa_next_free_sgpr 102
		.amdhsa_accum_offset 256
		.amdhsa_reserve_vcc 1
		.amdhsa_float_round_mode_32 0
		.amdhsa_float_round_mode_16_64 0
		.amdhsa_float_denorm_mode_32 3
		.amdhsa_float_denorm_mode_16_64 3
		.amdhsa_dx10_clamp 1
		.amdhsa_ieee_mode 1
		.amdhsa_fp16_overflow 0
		.amdhsa_tg_split 0
		.amdhsa_exception_fp_ieee_invalid_op 0
		.amdhsa_exception_fp_denorm_src 0
		.amdhsa_exception_fp_ieee_div_zero 0
		.amdhsa_exception_fp_ieee_overflow 0
		.amdhsa_exception_fp_ieee_underflow 0
		.amdhsa_exception_fp_ieee_inexact 0
		.amdhsa_exception_int_div_zero 0
	.end_amdhsa_kernel

; #define LAS __attribute__((address_space(3)))
; __global__ void __launch_bounds__(NWAVES * 64, 2) fwd_kernel(Args args) {
;     extern __shared__ __attribute__((aligned(16))) unsigned char lds_raw[];
;     LAS unsigned char* lds = (LAS unsigned char*)lds_raw;
;     volatile LAS unsigned* MISC = (volatile LAS unsigned*)(lds + MISC_OFF);
;     const int G0 = gridDim.x, bid0 = blockIdx.x;
;     const int wave_s = __builtin_amdgcn_readfirstlane(threadIdx.x >> 6);
amdhsa.kernels:
  - .agpr_count:     0
    .args:
      - .offset:         0
        .size:           320
        .value_kind:     by_value
      - .offset:         320
        .size:           4
        .value_kind:     hidden_block_count_x
      - .offset:         324
        .size:           4
        .value_kind:     hidden_block_count_y
      - .offset:         328
        .size:           4
        .value_kind:     hidden_block_count_z
      - .offset:         332
        .size:           2
        .value_kind:     hidden_group_size_x
      - .offset:         334
        .size:           2
        .value_kind:     hidden_group_size_y
      - .offset:         336
        .size:           2
        .value_kind:     hidden_group_size_z
      - .offset:         338
        .size:           2
        .value_kind:     hidden_remainder_x
      - .offset:         340
        .size:           2
        .value_kind:     hidden_remainder_y
      - .offset:         342
        .size:           2
        .value_kind:     hidden_remainder_z
      - .offset:         360
        .size:           8
        .value_kind:     hidden_global_offset_x
      - .offset:         368
        .size:           8
        .value_kind:     hidden_global_offset_y
      - .offset:         376
        .size:           8
        .value_kind:     hidden_global_offset_z
      - .offset:         384
        .size:           2
        .value_kind:     hidden_grid_dims
      - .offset:         440
        .size:           4
        .value_kind:     hidden_dynamic_lds_size
    .group_segment_fixed_size: 0
    .kernarg_segment_align: 8
    .kernarg_segment_size: 576
    .language:       OpenCL C
    .language_version:
      - 2
      - 0
    .max_flat_workgroup_size: 512
    .name:           _Z10fwd_kernel4Args
    .private_segment_fixed_size: 0
    .sgpr_count:     108
    .sgpr_spill_count: 177
    .symbol:         _Z10fwd_kernel4Args.kd
    .uniform_work_group_size: 1
    .uses_dynamic_stack: false
    .vgpr_count:     256
    .vgpr_spill_count: 0
    .wavefront_size: 64
